# speedup vs baseline: 1.0699x; 1.0070x over previous
_Z11main_kernelPKcPfS1_:
	s_load_dwordx2 s[6:7], s[0:1], 0x0
	s_and_b32 s3, s2, 7
	s_lshr_b32 s4, s2, 3
	s_and_b32 s5, s4, 3
	s_lshl_b32 s3, s3, 2
	s_or_b32 s8, s3, s5
	s_lshr_b32 s9, s4, 2
	v_lshrrev_b32_e32 v127, 6, v0
	v_and_b32_e32 v124, 63, v0
	v_lshlrev_b32_e32 v124, 4, v124
	v_mov_b32_e32 v120, 0
	v_readfirstlane_b32 s12, v127
	v_mov_b32_e32 v121, 0
	v_mov_b32_e32 v122, 0
	v_mov_b32_e32 v123, 0
	s_lshl_b32 s13, s12, 10
	s_lshl_b32 s14, s9, 3
	s_add_u32 s14, s14, s12
	s_lshl_b32 s15, s14, 13
	s_mul_i32 s16, s8, 0x18000
	s_add_u32 s16, s16, 0x100000
	v_or_b32_e32 v125, s13, v124
	v_or_b32_e32 v126, 0x2000, v125
	s_add_u32 s20, s13, 0x2000
	s_waitcnt lgkmcnt(0)
	s_add_u32 s10, s6, s16
	s_addc_u32 s11, s7, 0
	s_add_u32 s18, s6, s15
	s_addc_u32 s19, s7, 0
	s_add_u32 s22, s18, 0x1000
	s_addc_u32 s23, s19, 0
	s_mov_b32 m0, s13
	s_nop 0
	global_load_lds_dwordx4 v125, s[10:11]
	s_mov_b32 m0, s20
	s_nop 0
	global_load_lds_dwordx4 v126, s[10:11]
	global_load_dwordx4 v[96:99], v124, s[18:19]
	global_load_dwordx2 v[100:101], v124, s[18:19] offset:1024
	global_load_dwordx4 v[102:105], v124, s[18:19] offset:2048
	global_load_dwordx2 v[106:107], v124, s[18:19] offset:3072
	global_load_dwordx4 v[108:111], v124, s[22:23]
	global_load_dwordx2 v[112:113], v124, s[22:23] offset:1024
	global_load_dwordx4 v[114:117], v124, s[22:23] offset:2048
	global_load_dwordx2 v[118:119], v124, s[22:23] offset:3072
	s_add_u32 s24, s10, 0x4000
	s_addc_u32 s25, s11, 0
	s_add_u32 s26, s13, 0x4000
	s_mov_b32 m0, s26
	s_nop 0
	global_load_lds_dwordx4 v125, s[24:25]
	s_add_u32 s26, s20, 0x4000
	s_mov_b32 m0, s26
	s_nop 0
	global_load_lds_dwordx4 v126, s[24:25]
	s_add_u32 s24, s10, 0x8000
	s_addc_u32 s25, s11, 0
	s_add_u32 s26, s13, 0x8000
	s_mov_b32 m0, s26
	s_nop 0
	global_load_lds_dwordx4 v125, s[24:25]
	s_add_u32 s26, s20, 0x8000
	s_mov_b32 m0, s26
	s_nop 0
	global_load_lds_dwordx4 v126, s[24:25]
	s_add_u32 s24, s10, 0xc000
	s_addc_u32 s25, s11, 0
	s_add_u32 s26, s13, 0xc000
	s_mov_b32 m0, s26
	s_nop 0
	global_load_lds_dwordx4 v125, s[24:25]
	s_add_u32 s26, s20, 0xc000
	s_mov_b32 m0, s26
	s_nop 0
	global_load_lds_dwordx4 v126, s[24:25]
	s_waitcnt vmcnt(6)
	s_barrier
	ds_read_b128 v[0:3], v124
	ds_read_b64 v[4:5], v124 offset:1024
	ds_read_b128 v[6:9], v124 offset:2048
	ds_read_b64 v[10:11], v124 offset:3072
	ds_read_b128 v[12:15], v124 offset:4096
	ds_read_b64 v[16:17], v124 offset:5120
	ds_read_b128 v[18:21], v124 offset:6144
	ds_read_b64 v[22:23], v124 offset:7168
	s_waitcnt lgkmcnt(0)
	s_setprio 3
	v_mfma_f32_32x32x64_f8f6f4 v[48:63], v[0:5], v[96:101], 0 cbsz:2 blgp:2
	ds_read_b128 v[24:27], v124 offset:8192
	ds_read_b64 v[28:29], v124 offset:9216
	v_mfma_f32_32x32x64_f8f6f4 v[48:63], v[6:11], v[102:107], v[48:63] cbsz:2 blgp:2
	ds_read_b128 v[30:33], v124 offset:10240
	ds_read_b64 v[34:35], v124 offset:11264
	v_mfma_f32_32x32x64_f8f6f4 v[48:63], v[12:17], v[108:113], v[48:63] cbsz:2 blgp:2
	ds_read_b128 v[36:39], v124 offset:12288
	ds_read_b64 v[40:41], v124 offset:13312
	v_mfma_f32_32x32x64_f8f6f4 v[48:63], v[18:23], v[114:119], v[48:63] cbsz:2 blgp:2
	ds_read_b128 v[42:45], v124 offset:14336
	ds_read_b64 v[46:47], v124 offset:15360
	s_waitcnt vmcnt(4) lgkmcnt(0)
	s_barrier
	s_add_u32 s24, s10, 0x10000
	s_addc_u32 s25, s11, 0
	s_mov_b32 m0, s13
	s_nop 0
	global_load_lds_dwordx4 v125, s[24:25]
	s_mov_b32 m0, s20
	s_nop 0
	global_load_lds_dwordx4 v126, s[24:25]
	v_mfma_f32_32x32x64_f8f6f4 v[64:79], v[24:29], v[96:101], 0 cbsz:2 blgp:2
	ds_read_b128 v[0:3], v124 offset:16384
	ds_read_b64 v[4:5], v124 offset:17408
	ds_read_b128 v[6:9], v124 offset:18432
	ds_read_b64 v[10:11], v124 offset:19456
	ds_read_b128 v[24:27], v124 offset:24576
	ds_read_b64 v[28:29], v124 offset:25600
	v_mfma_f32_32x32x64_f8f6f4 v[64:79], v[30:35], v[102:107], v[64:79] cbsz:2 blgp:2
	ds_read_b128 v[12:15], v124 offset:20480
	ds_read_b64 v[16:17], v124 offset:21504
	ds_read_b128 v[18:21], v124 offset:22528
	ds_read_b64 v[22:23], v124 offset:23552
	ds_read_b128 v[30:33], v124 offset:26624
	ds_read_b64 v[34:35], v124 offset:27648
	v_exp_f32_e32 v48, v48
	v_exp_f32_e32 v49, v49
	v_exp_f32_e32 v50, v50
	v_exp_f32_e32 v51, v51
	v_mfma_f32_32x32x64_f8f6f4 v[64:79], v[36:41], v[108:113], v[64:79] cbsz:2 blgp:2
	ds_read_b128 v[36:39], v124 offset:28672
	ds_read_b64 v[40:41], v124 offset:29696
	v_exp_f32_e32 v52, v52
	v_exp_f32_e32 v53, v53
	v_exp_f32_e32 v54, v54
	v_exp_f32_e32 v55, v55
	v_pk_add_f32 v[120:121], v[120:121], v[48:49]
	v_pk_add_f32 v[122:123], v[122:123], v[50:51]
	v_mfma_f32_32x32x64_f8f6f4 v[64:79], v[42:47], v[114:119], v[64:79] cbsz:2 blgp:2
	ds_read_b128 v[42:45], v124 offset:30720
	ds_read_b64 v[46:47], v124 offset:31744
	v_exp_f32_e32 v56, v56
	v_exp_f32_e32 v57, v57
	v_exp_f32_e32 v58, v58
	v_exp_f32_e32 v59, v59
	v_pk_add_f32 v[120:121], v[120:121], v[52:53]
	v_pk_add_f32 v[122:123], v[122:123], v[54:55]
	s_waitcnt vmcnt(4) lgkmcnt(6)
	s_barrier
	v_mfma_f32_32x32x64_f8f6f4 v[80:95], v[0:5], v[96:101], 0 cbsz:2 blgp:2
	ds_read_b128 v[0:3], v124 offset:32768
	ds_read_b64 v[4:5], v124 offset:33792
	v_exp_f32_e32 v60, v60
	v_exp_f32_e32 v61, v61
	v_exp_f32_e32 v62, v62
	v_exp_f32_e32 v63, v63
	v_pk_add_f32 v[120:121], v[120:121], v[56:57]
	v_pk_add_f32 v[122:123], v[122:123], v[58:59]
	v_mfma_f32_32x32x64_f8f6f4 v[80:95], v[6:11], v[102:107], v[80:95] cbsz:2 blgp:2
	ds_read_b128 v[6:9], v124 offset:34816
	ds_read_b64 v[10:11], v124 offset:35840
	v_exp_f32_e32 v64, v64
	v_exp_f32_e32 v65, v65
	v_exp_f32_e32 v66, v66
	v_exp_f32_e32 v67, v67
	v_pk_add_f32 v[120:121], v[120:121], v[60:61]
	v_pk_add_f32 v[122:123], v[122:123], v[62:63]
	v_mfma_f32_32x32x64_f8f6f4 v[80:95], v[12:17], v[108:113], v[80:95] cbsz:2 blgp:2
	ds_read_b128 v[12:15], v124 offset:36864
	ds_read_b64 v[16:17], v124 offset:37888
	v_exp_f32_e32 v68, v68
	v_exp_f32_e32 v69, v69
	v_exp_f32_e32 v70, v70
	v_exp_f32_e32 v71, v71
	v_pk_add_f32 v[120:121], v[120:121], v[64:65]
	v_pk_add_f32 v[122:123], v[122:123], v[66:67]
	v_mfma_f32_32x32x64_f8f6f4 v[80:95], v[18:23], v[114:119], v[80:95] cbsz:2 blgp:2
	ds_read_b128 v[18:21], v124 offset:38912
	ds_read_b64 v[22:23], v124 offset:39936
	v_exp_f32_e32 v72, v72
	v_exp_f32_e32 v73, v73
	v_exp_f32_e32 v74, v74
	v_exp_f32_e32 v75, v75
	v_pk_add_f32 v[120:121], v[120:121], v[68:69]
	v_pk_add_f32 v[122:123], v[122:123], v[70:71]
	s_waitcnt lgkmcnt(8)
	v_mfma_f32_32x32x64_f8f6f4 v[48:63], v[24:29], v[96:101], 0 cbsz:2 blgp:2
	ds_read_b128 v[24:27], v124 offset:40960
	ds_read_b64 v[28:29], v124 offset:41984
	v_exp_f32_e32 v76, v76
	v_exp_f32_e32 v77, v77
	v_exp_f32_e32 v78, v78
	v_exp_f32_e32 v79, v79
	v_pk_add_f32 v[120:121], v[120:121], v[72:73]
	v_pk_add_f32 v[122:123], v[122:123], v[74:75]
	v_mfma_f32_32x32x64_f8f6f4 v[48:63], v[30:35], v[102:107], v[48:63] cbsz:2 blgp:2
	ds_read_b128 v[30:33], v124 offset:43008
	ds_read_b64 v[34:35], v124 offset:44032
	v_exp_f32_e32 v80, v80
	v_exp_f32_e32 v81, v81
	v_exp_f32_e32 v82, v82
	v_exp_f32_e32 v83, v83
	v_pk_add_f32 v[120:121], v[120:121], v[76:77]
	v_pk_add_f32 v[122:123], v[122:123], v[78:79]
	v_mfma_f32_32x32x64_f8f6f4 v[48:63], v[36:41], v[108:113], v[48:63] cbsz:2 blgp:2
	ds_read_b128 v[36:39], v124 offset:45056
	ds_read_b64 v[40:41], v124 offset:46080
	v_exp_f32_e32 v84, v84
	v_exp_f32_e32 v85, v85
	v_exp_f32_e32 v86, v86
	v_exp_f32_e32 v87, v87
	v_pk_add_f32 v[120:121], v[120:121], v[80:81]
	v_pk_add_f32 v[122:123], v[122:123], v[82:83]
	v_mfma_f32_32x32x64_f8f6f4 v[48:63], v[42:47], v[114:119], v[48:63] cbsz:2 blgp:2
	ds_read_b128 v[42:45], v124 offset:47104
	ds_read_b64 v[46:47], v124 offset:48128
	v_exp_f32_e32 v88, v88
	v_exp_f32_e32 v89, v89
	v_exp_f32_e32 v90, v90
	v_exp_f32_e32 v91, v91
	v_pk_add_f32 v[120:121], v[120:121], v[84:85]
	v_pk_add_f32 v[122:123], v[122:123], v[86:87]
	s_setprio 2
	s_waitcnt vmcnt(2) lgkmcnt(8)
	s_barrier
	s_add_u32 s24, s10, 0x14000
	s_addc_u32 s25, s11, 0
	s_add_u32 s26, s13, 0x4000
	s_mov_b32 m0, s26
	s_nop 0
	global_load_lds_dwordx4 v125, s[24:25]
	s_add_u32 s26, s20, 0x4000
	s_mov_b32 m0, s26
	s_nop 0
	global_load_lds_dwordx4 v126, s[24:25]
	v_mfma_f32_32x32x64_f8f6f4 v[64:79], v[0:5], v[96:101], 0 cbsz:2 blgp:2
	ds_read_b128 v[0:3], v124 offset:49152
	ds_read_b64 v[4:5], v124 offset:50176
	v_exp_f32_e32 v92, v92
	v_exp_f32_e32 v93, v93
	v_exp_f32_e32 v94, v94
	v_exp_f32_e32 v95, v95
	v_pk_add_f32 v[120:121], v[120:121], v[88:89]
	v_pk_add_f32 v[122:123], v[122:123], v[90:91]
	v_mfma_f32_32x32x64_f8f6f4 v[64:79], v[6:11], v[102:107], v[64:79] cbsz:2 blgp:2
	ds_read_b128 v[6:9], v124 offset:51200
	ds_read_b64 v[10:11], v124 offset:52224
	v_exp_f32_e32 v48, v48
	v_exp_f32_e32 v49, v49
	v_exp_f32_e32 v50, v50
	v_exp_f32_e32 v51, v51
	v_pk_add_f32 v[120:121], v[120:121], v[92:93]
	v_pk_add_f32 v[122:123], v[122:123], v[94:95]
	v_mfma_f32_32x32x64_f8f6f4 v[64:79], v[12:17], v[108:113], v[64:79] cbsz:2 blgp:2
	ds_read_b128 v[12:15], v124 offset:53248
	ds_read_b64 v[16:17], v124 offset:54272
	v_exp_f32_e32 v52, v52
	v_exp_f32_e32 v53, v53
	v_exp_f32_e32 v54, v54
	v_exp_f32_e32 v55, v55
	v_pk_add_f32 v[120:121], v[120:121], v[48:49]
	v_pk_add_f32 v[122:123], v[122:123], v[50:51]
	v_mfma_f32_32x32x64_f8f6f4 v[64:79], v[18:23], v[114:119], v[64:79] cbsz:2 blgp:2
	ds_read_b128 v[18:21], v124 offset:55296
	ds_read_b64 v[22:23], v124 offset:56320
	v_exp_f32_e32 v56, v56
	v_exp_f32_e32 v57, v57
	v_exp_f32_e32 v58, v58
	v_exp_f32_e32 v59, v59
	v_pk_add_f32 v[120:121], v[120:121], v[52:53]
	v_pk_add_f32 v[122:123], v[122:123], v[54:55]
	s_waitcnt lgkmcnt(8)
	v_mfma_f32_32x32x64_f8f6f4 v[80:95], v[24:29], v[96:101], 0 cbsz:2 blgp:2
	ds_read_b128 v[24:27], v124 offset:57344
	ds_read_b64 v[28:29], v124 offset:58368
	v_exp_f32_e32 v60, v60
	v_exp_f32_e32 v61, v61
	v_exp_f32_e32 v62, v62
	v_exp_f32_e32 v63, v63
	v_pk_add_f32 v[120:121], v[120:121], v[56:57]
	v_pk_add_f32 v[122:123], v[122:123], v[58:59]
	v_mfma_f32_32x32x64_f8f6f4 v[80:95], v[30:35], v[102:107], v[80:95] cbsz:2 blgp:2
	ds_read_b128 v[30:33], v124 offset:59392
	ds_read_b64 v[34:35], v124 offset:60416
	v_exp_f32_e32 v64, v64
	v_exp_f32_e32 v65, v65
	v_exp_f32_e32 v66, v66
	v_exp_f32_e32 v67, v67
	v_pk_add_f32 v[120:121], v[120:121], v[60:61]
	v_pk_add_f32 v[122:123], v[122:123], v[62:63]
	v_mfma_f32_32x32x64_f8f6f4 v[80:95], v[36:41], v[108:113], v[80:95] cbsz:2 blgp:2
	ds_read_b128 v[36:39], v124 offset:61440
	ds_read_b64 v[40:41], v124 offset:62464
	v_exp_f32_e32 v68, v68
	v_exp_f32_e32 v69, v69
	v_exp_f32_e32 v70, v70
	v_exp_f32_e32 v71, v71
	v_pk_add_f32 v[120:121], v[120:121], v[64:65]
	v_pk_add_f32 v[122:123], v[122:123], v[66:67]
	v_mfma_f32_32x32x64_f8f6f4 v[80:95], v[42:47], v[114:119], v[80:95] cbsz:2 blgp:2
	ds_read_b128 v[42:45], v124 offset:63488
	ds_read_b64 v[46:47], v124 offset:64512
	v_exp_f32_e32 v72, v72
	v_exp_f32_e32 v73, v73
	v_exp_f32_e32 v74, v74
	v_exp_f32_e32 v75, v75
	v_pk_add_f32 v[120:121], v[120:121], v[68:69]
	v_pk_add_f32 v[122:123], v[122:123], v[70:71]
	s_waitcnt vmcnt(2) lgkmcnt(8)
	s_barrier
	v_mfma_f32_32x32x64_f8f6f4 v[48:63], v[0:5], v[96:101], 0 cbsz:2 blgp:2
	ds_read_b128 v[0:3], v124
	ds_read_b64 v[4:5], v124 offset:1024
	v_exp_f32_e32 v76, v76
	v_exp_f32_e32 v77, v77
	v_exp_f32_e32 v78, v78
	v_exp_f32_e32 v79, v79
	v_pk_add_f32 v[120:121], v[120:121], v[72:73]
	v_pk_add_f32 v[122:123], v[122:123], v[74:75]
	v_mfma_f32_32x32x64_f8f6f4 v[48:63], v[6:11], v[102:107], v[48:63] cbsz:2 blgp:2
	ds_read_b128 v[6:9], v124 offset:2048
	ds_read_b64 v[10:11], v124 offset:3072
	v_exp_f32_e32 v80, v80
	v_exp_f32_e32 v81, v81
	v_exp_f32_e32 v82, v82
	v_exp_f32_e32 v83, v83
	v_pk_add_f32 v[120:121], v[120:121], v[76:77]
	v_pk_add_f32 v[122:123], v[122:123], v[78:79]
	v_mfma_f32_32x32x64_f8f6f4 v[48:63], v[12:17], v[108:113], v[48:63] cbsz:2 blgp:2
	ds_read_b128 v[12:15], v124 offset:4096
	ds_read_b64 v[16:17], v124 offset:5120
	v_exp_f32_e32 v84, v84
	v_exp_f32_e32 v85, v85
	v_exp_f32_e32 v86, v86
	v_exp_f32_e32 v87, v87
	v_pk_add_f32 v[120:121], v[120:121], v[80:81]
	v_pk_add_f32 v[122:123], v[122:123], v[82:83]
	v_mfma_f32_32x32x64_f8f6f4 v[48:63], v[18:23], v[114:119], v[48:63] cbsz:2 blgp:2
	ds_read_b128 v[18:21], v124 offset:6144
	ds_read_b64 v[22:23], v124 offset:7168
	v_exp_f32_e32 v88, v88
	v_exp_f32_e32 v89, v89
	v_exp_f32_e32 v90, v90
	v_exp_f32_e32 v91, v91
	v_pk_add_f32 v[120:121], v[120:121], v[84:85]
	v_pk_add_f32 v[122:123], v[122:123], v[86:87]
	s_waitcnt lgkmcnt(8)
	v_mfma_f32_32x32x64_f8f6f4 v[64:79], v[24:29], v[96:101], 0 cbsz:2 blgp:2
	ds_read_b128 v[24:27], v124 offset:8192
	ds_read_b64 v[28:29], v124 offset:9216
	v_exp_f32_e32 v92, v92
	v_exp_f32_e32 v93, v93
	v_exp_f32_e32 v94, v94
	v_exp_f32_e32 v95, v95
	v_pk_add_f32 v[120:121], v[120:121], v[88:89]
	v_pk_add_f32 v[122:123], v[122:123], v[90:91]
	v_mfma_f32_32x32x64_f8f6f4 v[64:79], v[30:35], v[102:107], v[64:79] cbsz:2 blgp:2
	ds_read_b128 v[30:33], v124 offset:10240
	ds_read_b64 v[34:35], v124 offset:11264
	v_exp_f32_e32 v48, v48
	v_exp_f32_e32 v49, v49
	v_exp_f32_e32 v50, v50
	v_exp_f32_e32 v51, v51
	v_pk_add_f32 v[120:121], v[120:121], v[92:93]
	v_pk_add_f32 v[122:123], v[122:123], v[94:95]
	v_mfma_f32_32x32x64_f8f6f4 v[64:79], v[36:41], v[108:113], v[64:79] cbsz:2 blgp:2
	ds_read_b128 v[36:39], v124 offset:12288
	ds_read_b64 v[40:41], v124 offset:13312
	v_exp_f32_e32 v52, v52
	v_exp_f32_e32 v53, v53
	v_exp_f32_e32 v54, v54
	v_exp_f32_e32 v55, v55
	v_pk_add_f32 v[120:121], v[120:121], v[48:49]
	v_pk_add_f32 v[122:123], v[122:123], v[50:51]
	v_mfma_f32_32x32x64_f8f6f4 v[64:79], v[42:47], v[114:119], v[64:79] cbsz:2 blgp:2
	ds_read_b128 v[42:45], v124 offset:14336
	ds_read_b64 v[46:47], v124 offset:15360
	v_exp_f32_e32 v56, v56
	v_exp_f32_e32 v57, v57
	v_exp_f32_e32 v58, v58
	v_exp_f32_e32 v59, v59
	v_pk_add_f32 v[120:121], v[120:121], v[52:53]
	v_pk_add_f32 v[122:123], v[122:123], v[54:55]
	s_setprio 1
	s_waitcnt vmcnt(0) lgkmcnt(8)
	s_barrier
	v_mfma_f32_32x32x64_f8f6f4 v[80:95], v[0:5], v[96:101], 0 cbsz:2 blgp:2
	ds_read_b128 v[0:3], v124 offset:16384
	ds_read_b64 v[4:5], v124 offset:17408
	v_exp_f32_e32 v60, v60
	v_exp_f32_e32 v61, v61
	v_exp_f32_e32 v62, v62
	v_exp_f32_e32 v63, v63
	v_pk_add_f32 v[120:121], v[120:121], v[56:57]
	v_pk_add_f32 v[122:123], v[122:123], v[58:59]
	v_mfma_f32_32x32x64_f8f6f4 v[80:95], v[6:11], v[102:107], v[80:95] cbsz:2 blgp:2
	ds_read_b128 v[6:9], v124 offset:18432
	ds_read_b64 v[10:11], v124 offset:19456
	v_exp_f32_e32 v64, v64
	v_exp_f32_e32 v65, v65
	v_exp_f32_e32 v66, v66
	v_exp_f32_e32 v67, v67
	v_pk_add_f32 v[120:121], v[120:121], v[60:61]
	v_pk_add_f32 v[122:123], v[122:123], v[62:63]
	v_mfma_f32_32x32x64_f8f6f4 v[80:95], v[12:17], v[108:113], v[80:95] cbsz:2 blgp:2
	ds_read_b128 v[12:15], v124 offset:20480
	ds_read_b64 v[16:17], v124 offset:21504
	v_exp_f32_e32 v68, v68
	v_exp_f32_e32 v69, v69
	v_exp_f32_e32 v70, v70
	v_exp_f32_e32 v71, v71
	v_pk_add_f32 v[120:121], v[120:121], v[64:65]
	v_pk_add_f32 v[122:123], v[122:123], v[66:67]
	v_mfma_f32_32x32x64_f8f6f4 v[80:95], v[18:23], v[114:119], v[80:95] cbsz:2 blgp:2
	ds_read_b128 v[18:21], v124 offset:22528
	ds_read_b64 v[22:23], v124 offset:23552
	v_exp_f32_e32 v72, v72
	v_exp_f32_e32 v73, v73
	v_exp_f32_e32 v74, v74
	v_exp_f32_e32 v75, v75
	v_pk_add_f32 v[120:121], v[120:121], v[68:69]
	v_pk_add_f32 v[122:123], v[122:123], v[70:71]
	s_waitcnt lgkmcnt(8)
	v_mfma_f32_32x32x64_f8f6f4 v[48:63], v[24:29], v[96:101], 0 cbsz:2 blgp:2
	ds_read_b128 v[24:27], v124 offset:24576
	ds_read_b64 v[28:29], v124 offset:25600
	v_exp_f32_e32 v76, v76
	v_exp_f32_e32 v77, v77
	v_exp_f32_e32 v78, v78
	v_exp_f32_e32 v79, v79
	v_pk_add_f32 v[120:121], v[120:121], v[72:73]
	v_pk_add_f32 v[122:123], v[122:123], v[74:75]
	v_mfma_f32_32x32x64_f8f6f4 v[48:63], v[30:35], v[102:107], v[48:63] cbsz:2 blgp:2
	ds_read_b128 v[30:33], v124 offset:26624
	ds_read_b64 v[34:35], v124 offset:27648
	v_exp_f32_e32 v80, v80
	v_exp_f32_e32 v81, v81
	v_exp_f32_e32 v82, v82
	v_exp_f32_e32 v83, v83
	v_pk_add_f32 v[120:121], v[120:121], v[76:77]
	v_pk_add_f32 v[122:123], v[122:123], v[78:79]
	s_cmp_lg_u32 s8, 10
	s_cbranch_scc1 .Lmk_nosplit
	v_add_f32_e32 v127, v120, v121
	v_add_f32_e32 v125, v122, v123
	v_mov_b32_e32 v120, 0
	v_mov_b32_e32 v121, 0
	v_mov_b32_e32 v122, 0
	v_mov_b32_e32 v123, 0
	v_add_f32_e32 v127, v127, v125
.Lmk_nosplit:
	v_mfma_f32_32x32x64_f8f6f4 v[48:63], v[36:41], v[108:113], v[48:63] cbsz:2 blgp:2
	ds_read_b128 v[36:39], v124 offset:28672
	ds_read_b64 v[40:41], v124 offset:29696
	v_exp_f32_e32 v84, v84
	v_exp_f32_e32 v85, v85
	v_exp_f32_e32 v86, v86
	v_exp_f32_e32 v87, v87
	v_pk_add_f32 v[120:121], v[120:121], v[80:81]
	v_pk_add_f32 v[122:123], v[122:123], v[82:83]
	v_mfma_f32_32x32x64_f8f6f4 v[48:63], v[42:47], v[114:119], v[48:63] cbsz:2 blgp:2
	ds_read_b128 v[42:45], v124 offset:30720
	ds_read_b64 v[46:47], v124 offset:31744
	v_exp_f32_e32 v88, v88
	v_exp_f32_e32 v89, v89
	v_exp_f32_e32 v90, v90
	v_exp_f32_e32 v91, v91
	v_pk_add_f32 v[120:121], v[120:121], v[84:85]
	v_pk_add_f32 v[122:123], v[122:123], v[86:87]
	s_setprio 0
	s_waitcnt lgkmcnt(8)
	v_mfma_f32_32x32x64_f8f6f4 v[64:79], v[0:5], v[96:101], 0 cbsz:2 blgp:2
	v_exp_f32_e32 v92, v92
	v_exp_f32_e32 v93, v93
	v_exp_f32_e32 v94, v94
	v_exp_f32_e32 v95, v95
	v_pk_add_f32 v[120:121], v[120:121], v[88:89]
	v_pk_add_f32 v[122:123], v[122:123], v[90:91]
	v_mfma_f32_32x32x64_f8f6f4 v[64:79], v[6:11], v[102:107], v[64:79] cbsz:2 blgp:2
	v_exp_f32_e32 v48, v48
	v_exp_f32_e32 v49, v49
	v_exp_f32_e32 v50, v50
	v_exp_f32_e32 v51, v51
	v_pk_add_f32 v[120:121], v[120:121], v[92:93]
	v_pk_add_f32 v[122:123], v[122:123], v[94:95]
	v_mfma_f32_32x32x64_f8f6f4 v[64:79], v[12:17], v[108:113], v[64:79] cbsz:2 blgp:2
	v_exp_f32_e32 v52, v52
	v_exp_f32_e32 v53, v53
	v_exp_f32_e32 v54, v54
	v_exp_f32_e32 v55, v55
	v_pk_add_f32 v[120:121], v[120:121], v[48:49]
	v_pk_add_f32 v[122:123], v[122:123], v[50:51]
	v_mfma_f32_32x32x64_f8f6f4 v[64:79], v[18:23], v[114:119], v[64:79] cbsz:2 blgp:2
	v_exp_f32_e32 v56, v56
	v_exp_f32_e32 v57, v57
	v_exp_f32_e32 v58, v58
	v_exp_f32_e32 v59, v59
	v_pk_add_f32 v[120:121], v[120:121], v[52:53]
	v_pk_add_f32 v[122:123], v[122:123], v[54:55]
	s_waitcnt lgkmcnt(0)
	v_mfma_f32_32x32x64_f8f6f4 v[80:95], v[24:29], v[96:101], 0 cbsz:2 blgp:2
	v_exp_f32_e32 v60, v60
	v_exp_f32_e32 v61, v61
	v_exp_f32_e32 v62, v62
	v_exp_f32_e32 v63, v63
	v_pk_add_f32 v[120:121], v[120:121], v[56:57]
	v_pk_add_f32 v[122:123], v[122:123], v[58:59]
	v_mfma_f32_32x32x64_f8f6f4 v[80:95], v[30:35], v[102:107], v[80:95] cbsz:2 blgp:2
	v_exp_f32_e32 v64, v64
	v_exp_f32_e32 v65, v65
	v_exp_f32_e32 v66, v66
	v_exp_f32_e32 v67, v67
	v_pk_add_f32 v[120:121], v[120:121], v[60:61]
	v_pk_add_f32 v[122:123], v[122:123], v[62:63]
	v_mfma_f32_32x32x64_f8f6f4 v[80:95], v[36:41], v[108:113], v[80:95] cbsz:2 blgp:2
	v_exp_f32_e32 v68, v68
	v_exp_f32_e32 v69, v69
	v_exp_f32_e32 v70, v70
	v_exp_f32_e32 v71, v71
	v_pk_add_f32 v[120:121], v[120:121], v[64:65]
	v_pk_add_f32 v[122:123], v[122:123], v[66:67]
	v_mfma_f32_32x32x64_f8f6f4 v[80:95], v[42:47], v[114:119], v[80:95] cbsz:2 blgp:2
	v_exp_f32_e32 v72, v72
	v_exp_f32_e32 v73, v73
	v_exp_f32_e32 v74, v74
	v_exp_f32_e32 v75, v75
	v_pk_add_f32 v[120:121], v[120:121], v[68:69]
	v_pk_add_f32 v[122:123], v[122:123], v[70:71]
	v_exp_f32_e32 v76, v76
	v_exp_f32_e32 v77, v77
	v_exp_f32_e32 v78, v78
	v_exp_f32_e32 v79, v79
	v_pk_add_f32 v[120:121], v[120:121], v[72:73]
	v_pk_add_f32 v[122:123], v[122:123], v[74:75]
	s_nop 1
	v_exp_f32_e32 v80, v80
	v_exp_f32_e32 v81, v81
	v_exp_f32_e32 v82, v82
	v_exp_f32_e32 v83, v83
	v_pk_add_f32 v[120:121], v[120:121], v[76:77]
	v_pk_add_f32 v[122:123], v[122:123], v[78:79]
	v_exp_f32_e32 v84, v84
	v_exp_f32_e32 v85, v85
	v_exp_f32_e32 v86, v86
	v_exp_f32_e32 v87, v87
	v_pk_add_f32 v[120:121], v[120:121], v[80:81]
	v_pk_add_f32 v[122:123], v[122:123], v[82:83]
	v_exp_f32_e32 v88, v88
	v_exp_f32_e32 v89, v89
	v_exp_f32_e32 v90, v90
	v_exp_f32_e32 v91, v91
	v_pk_add_f32 v[120:121], v[120:121], v[84:85]
	v_pk_add_f32 v[122:123], v[122:123], v[86:87]
	v_exp_f32_e32 v92, v92
	v_exp_f32_e32 v93, v93
	v_exp_f32_e32 v94, v94
	v_exp_f32_e32 v95, v95
	v_pk_add_f32 v[120:121], v[120:121], v[88:89]
	v_pk_add_f32 v[122:123], v[122:123], v[90:91]
	v_pk_add_f32 v[120:121], v[120:121], v[92:93]
	v_pk_add_f32 v[122:123], v[122:123], v[94:95]
	v_add_f32_e32 v120, v120, v121
	v_add_f32_e32 v122, v122, v123
	v_lshrrev_b32_e32 v126, 2, v124
	v_add_f32_e32 v120, v120, v122
	v_xor_b32_e32 v125, 0x80, v126
	s_load_dwordx4 s[4:7], s[0:1], 0x8
	ds_bpermute_b32 v122, v125, v120
	ds_bpermute_b32 v123, v125, v127
	s_lshl_b32 s14, s14, 7
	v_add_u32_e32 v126, s14, v126
	v_cmp_gt_u32_e32 vcc, 0x200, v124
	s_and_saveexec_b64 s[16:17], vcc
	s_cbranch_execz .Lmk_end
	s_waitcnt lgkmcnt(0)
	v_add_f32_e32 v120, v120, v122
	v_add_f32_e32 v127, v127, v123
	s_cmp_lt_u32 s8, 10
	s_cbranch_scc1 .Lmk_pos_only
	s_cmp_eq_u32 s8, 10
	s_cbranch_scc0 .Lmk_neg_only
	global_atomic_add_f32 v126, v127, s[4:5]
